# router half-trips: counted waits split per quarter-trip (first four operand loads, then the next four)
# baseline (speedup 1.0000x reference)
.LBB0_711:
	v_lshl_add_u64 v[52:53], v[50:51], 0, s[12:13]
	v_add_co_u32_e32 v152, vcc, s42, v52
	v_lshl_add_u64 v[54:55], v[48:49], 0, s[12:13]
	s_nop 0
	v_addc_co_u32_e32 v153, vcc, 0, v53, vcc
	v_add_co_u32_e32 v154, vcc, s45, v52
	s_nop 0
	s_nop 0
	v_addc_co_u32_e32 v155, vcc, 0, v53, vcc
	v_add_co_u32_e32 v156, vcc, s46, v54
	s_nop 0
	s_nop 0
	v_addc_co_u32_e32 v157, vcc, 0, v55, vcc
	v_add_co_u32_e32 v158, vcc, s47, v54
	s_nop 0
	s_nop 0
	v_addc_co_u32_e32 v159, vcc, 0, v55, vcc
	global_load_dwordx4 v[176:179], v[152:153], off
	global_load_dwordx4 v[180:183], v[156:157], off
	global_load_dwordx4 v[184:187], v[154:155], off
	global_load_dwordx4 v[188:191], v[158:159], off
	global_load_dwordx4 v[192:195], v[152:153], off offset:32
	global_load_dwordx4 v[196:199], v[156:157], off offset:32
	global_load_dwordx4 v[200:203], v[154:155], off offset:32
	global_load_dwordx4 v[204:207], v[158:159], off offset:32
	global_load_dwordx4 v[208:211], v[152:153], off offset:64
	global_load_dwordx4 v[212:215], v[156:157], off offset:64
	global_load_dwordx4 v[216:219], v[154:155], off offset:64
	global_load_dwordx4 v[220:223], v[158:159], off offset:64
	global_load_dwordx4 v[224:227], v[152:153], off offset:96
	global_load_dwordx4 v[228:231], v[156:157], off offset:96
	global_load_dwordx4 v[232:235], v[154:155], off offset:96
	global_load_dwordx4 v[236:239], v[158:159], off offset:96
	global_load_dwordx4 v[240:243], v[152:153], off offset:128
	global_load_dwordx4 v[244:247], v[156:157], off offset:128
	global_load_dwordx4 v[248:251], v[154:155], off offset:128
	global_load_dwordx4 v[52:55], v[158:159], off offset:128
	global_load_dwordx4 v[56:59], v[152:153], off offset:160
	global_load_dwordx4 v[60:63], v[156:157], off offset:160
	global_load_dwordx4 v[64:67], v[154:155], off offset:160
	global_load_dwordx4 v[68:71], v[158:159], off offset:160
	s_waitcnt vmcnt(20)
	v_mfma_f32_32x32x16_bf16 v[2:17], v[176:179], v[180:183], v[2:17]
	v_mfma_f32_32x32x16_bf16 v[18:33], v[184:187], v[180:183], v[18:33]
	v_mfma_f32_32x32x16_bf16 v[2:17], v[176:179], v[188:191], v[2:17]
	v_mfma_f32_32x32x16_bf16 v[18:33], v[184:187], v[188:191], v[18:33]
	s_waitcnt vmcnt(16)
	v_mfma_f32_32x32x16_bf16 v[2:17], v[192:195], v[196:199], v[2:17]
	v_mfma_f32_32x32x16_bf16 v[18:33], v[200:203], v[196:199], v[18:33]
	v_mfma_f32_32x32x16_bf16 v[2:17], v[192:195], v[204:207], v[2:17]
	v_mfma_f32_32x32x16_bf16 v[18:33], v[200:203], v[204:207], v[18:33]
	global_load_dwordx4 v[176:179], v[152:153], off offset:192
	global_load_dwordx4 v[180:183], v[156:157], off offset:192
	global_load_dwordx4 v[184:187], v[154:155], off offset:192
	global_load_dwordx4 v[188:191], v[158:159], off offset:192
	global_load_dwordx4 v[192:195], v[152:153], off offset:224
	global_load_dwordx4 v[196:199], v[156:157], off offset:224
	global_load_dwordx4 v[200:203], v[154:155], off offset:224
	global_load_dwordx4 v[204:207], v[158:159], off offset:224
	s_waitcnt vmcnt(20)
	v_mfma_f32_32x32x16_bf16 v[2:17], v[208:211], v[212:215], v[2:17]
	v_mfma_f32_32x32x16_bf16 v[18:33], v[216:219], v[212:215], v[18:33]
	v_mfma_f32_32x32x16_bf16 v[2:17], v[208:211], v[220:223], v[2:17]
	v_mfma_f32_32x32x16_bf16 v[18:33], v[216:219], v[220:223], v[18:33]
	s_waitcnt vmcnt(16)
	v_mfma_f32_32x32x16_bf16 v[2:17], v[224:227], v[228:231], v[2:17]
	v_mfma_f32_32x32x16_bf16 v[18:33], v[232:235], v[228:231], v[18:33]
	v_mfma_f32_32x32x16_bf16 v[2:17], v[224:227], v[236:239], v[2:17]
	v_mfma_f32_32x32x16_bf16 v[18:33], v[232:235], v[236:239], v[18:33]
	global_load_dwordx4 v[208:211], v[152:153], off offset:256
	global_load_dwordx4 v[212:215], v[156:157], off offset:256
	global_load_dwordx4 v[216:219], v[154:155], off offset:256
	global_load_dwordx4 v[220:223], v[158:159], off offset:256
	global_load_dwordx4 v[224:227], v[152:153], off offset:288
	global_load_dwordx4 v[228:231], v[156:157], off offset:288
	global_load_dwordx4 v[232:235], v[154:155], off offset:288
	global_load_dwordx4 v[236:239], v[158:159], off offset:288
	s_waitcnt vmcnt(20)
	v_mfma_f32_32x32x16_bf16 v[2:17], v[240:243], v[244:247], v[2:17]
	v_mfma_f32_32x32x16_bf16 v[18:33], v[248:251], v[244:247], v[18:33]
	v_mfma_f32_32x32x16_bf16 v[2:17], v[240:243], v[52:55], v[2:17]
	v_mfma_f32_32x32x16_bf16 v[18:33], v[248:251], v[52:55], v[18:33]
	s_waitcnt vmcnt(16)
	v_mfma_f32_32x32x16_bf16 v[2:17], v[56:59], v[60:63], v[2:17]
	v_mfma_f32_32x32x16_bf16 v[18:33], v[64:67], v[60:63], v[18:33]
	v_mfma_f32_32x32x16_bf16 v[2:17], v[56:59], v[68:71], v[2:17]
	v_mfma_f32_32x32x16_bf16 v[18:33], v[64:67], v[68:71], v[18:33]
	global_load_dwordx4 v[240:243], v[152:153], off offset:320
	global_load_dwordx4 v[244:247], v[156:157], off offset:320
	global_load_dwordx4 v[248:251], v[154:155], off offset:320
	global_load_dwordx4 v[52:55], v[158:159], off offset:320
	global_load_dwordx4 v[56:59], v[152:153], off offset:352
	global_load_dwordx4 v[60:63], v[156:157], off offset:352
	global_load_dwordx4 v[64:67], v[154:155], off offset:352
	global_load_dwordx4 v[68:71], v[158:159], off offset:352
	s_waitcnt vmcnt(20)
	v_mfma_f32_32x32x16_bf16 v[2:17], v[176:179], v[180:183], v[2:17]
	v_mfma_f32_32x32x16_bf16 v[18:33], v[184:187], v[180:183], v[18:33]
	v_mfma_f32_32x32x16_bf16 v[2:17], v[176:179], v[188:191], v[2:17]
	v_mfma_f32_32x32x16_bf16 v[18:33], v[184:187], v[188:191], v[18:33]
	s_waitcnt vmcnt(16)
	v_mfma_f32_32x32x16_bf16 v[2:17], v[192:195], v[196:199], v[2:17]
	v_mfma_f32_32x32x16_bf16 v[18:33], v[200:203], v[196:199], v[18:33]
	v_mfma_f32_32x32x16_bf16 v[2:17], v[192:195], v[204:207], v[2:17]
	v_mfma_f32_32x32x16_bf16 v[18:33], v[200:203], v[204:207], v[18:33]
	global_load_dwordx4 v[176:179], v[152:153], off offset:384
	global_load_dwordx4 v[180:183], v[156:157], off offset:384
	global_load_dwordx4 v[184:187], v[154:155], off offset:384
	global_load_dwordx4 v[188:191], v[158:159], off offset:384
	global_load_dwordx4 v[192:195], v[152:153], off offset:416
	global_load_dwordx4 v[196:199], v[156:157], off offset:416
	global_load_dwordx4 v[200:203], v[154:155], off offset:416
	global_load_dwordx4 v[204:207], v[158:159], off offset:416
	s_waitcnt vmcnt(20)
	v_mfma_f32_32x32x16_bf16 v[2:17], v[208:211], v[212:215], v[2:17]
	v_mfma_f32_32x32x16_bf16 v[18:33], v[216:219], v[212:215], v[18:33]
	v_mfma_f32_32x32x16_bf16 v[2:17], v[208:211], v[220:223], v[2:17]
	v_mfma_f32_32x32x16_bf16 v[18:33], v[216:219], v[220:223], v[18:33]
	s_waitcnt vmcnt(16)
	v_mfma_f32_32x32x16_bf16 v[2:17], v[224:227], v[228:231], v[2:17]
	v_mfma_f32_32x32x16_bf16 v[18:33], v[232:235], v[228:231], v[18:33]
	v_mfma_f32_32x32x16_bf16 v[2:17], v[224:227], v[236:239], v[2:17]
	v_mfma_f32_32x32x16_bf16 v[18:33], v[232:235], v[236:239], v[18:33]
	global_load_dwordx4 v[208:211], v[152:153], off offset:448
	global_load_dwordx4 v[212:215], v[156:157], off offset:448
	global_load_dwordx4 v[216:219], v[154:155], off offset:448
	global_load_dwordx4 v[220:223], v[158:159], off offset:448
	global_load_dwordx4 v[224:227], v[152:153], off offset:480
	global_load_dwordx4 v[228:231], v[156:157], off offset:480
	global_load_dwordx4 v[232:235], v[154:155], off offset:480
	global_load_dwordx4 v[236:239], v[158:159], off offset:480
	s_waitcnt vmcnt(20)
	v_mfma_f32_32x32x16_bf16 v[2:17], v[240:243], v[244:247], v[2:17]
	v_mfma_f32_32x32x16_bf16 v[18:33], v[248:251], v[244:247], v[18:33]
	v_mfma_f32_32x32x16_bf16 v[2:17], v[240:243], v[52:55], v[2:17]
	v_mfma_f32_32x32x16_bf16 v[18:33], v[248:251], v[52:55], v[18:33]
	s_waitcnt vmcnt(16)
	v_mfma_f32_32x32x16_bf16 v[2:17], v[56:59], v[60:63], v[2:17]
	v_mfma_f32_32x32x16_bf16 v[18:33], v[64:67], v[60:63], v[18:33]
	v_mfma_f32_32x32x16_bf16 v[2:17], v[56:59], v[68:71], v[2:17]
	v_mfma_f32_32x32x16_bf16 v[18:33], v[64:67], v[68:71], v[18:33]
	s_waitcnt vmcnt(12)
	v_mfma_f32_32x32x16_bf16 v[2:17], v[176:179], v[180:183], v[2:17]
	v_mfma_f32_32x32x16_bf16 v[18:33], v[184:187], v[180:183], v[18:33]
	v_mfma_f32_32x32x16_bf16 v[2:17], v[176:179], v[188:191], v[2:17]
	v_mfma_f32_32x32x16_bf16 v[18:33], v[184:187], v[188:191], v[18:33]
	s_waitcnt vmcnt(8)
	v_mfma_f32_32x32x16_bf16 v[2:17], v[192:195], v[196:199], v[2:17]
	v_mfma_f32_32x32x16_bf16 v[18:33], v[200:203], v[196:199], v[18:33]
	v_mfma_f32_32x32x16_bf16 v[2:17], v[192:195], v[204:207], v[2:17]
	v_mfma_f32_32x32x16_bf16 v[18:33], v[200:203], v[204:207], v[18:33]
	s_waitcnt vmcnt(4)
	v_mfma_f32_32x32x16_bf16 v[2:17], v[208:211], v[212:215], v[2:17]
	v_mfma_f32_32x32x16_bf16 v[18:33], v[216:219], v[212:215], v[18:33]
	v_mfma_f32_32x32x16_bf16 v[2:17], v[208:211], v[220:223], v[2:17]
	v_mfma_f32_32x32x16_bf16 v[18:33], v[216:219], v[220:223], v[18:33]
	s_waitcnt vmcnt(0)
	v_mfma_f32_32x32x16_bf16 v[2:17], v[224:227], v[228:231], v[2:17]
	v_mfma_f32_32x32x16_bf16 v[18:33], v[232:235], v[228:231], v[18:33]
	v_mfma_f32_32x32x16_bf16 v[2:17], v[224:227], v[236:239], v[2:17]
	v_mfma_f32_32x32x16_bf16 v[18:33], v[232:235], v[236:239], v[18:33]
	s_movk_i32 s12, 0x200
	s_mov_b32 s13, 0
	s_cmpk_eq_i32 s12, 0x200
	s_nop 9
	ds_write2_b32 v74, v2, v3 offset1:32
	v_add_u32_e32 v2, 0x1000, v74
	ds_write2_b32 v2, v18, v19 offset1:32
	ds_write2_b32 v74, v4, v5 offset0:64 offset1:96
	ds_write2_b32 v2, v20, v21 offset0:64 offset1:96
	v_add_u32_e32 v2, 0x400, v74
	v_add_u32_e32 v3, 0x1400, v74
	ds_write2_b32 v2, v6, v7 offset1:32
	ds_write2_b32 v3, v22, v23 offset1:32
	ds_write2_b32 v2, v8, v9 offset0:64 offset1:96
	ds_write2_b32 v3, v24, v25 offset0:64 offset1:96
	v_add_u32_e32 v2, 0x800, v74
	v_add_u32_e32 v3, 0x1800, v74
	ds_write2_b32 v2, v10, v11 offset1:32
	ds_write2_b32 v3, v26, v27 offset1:32
	ds_write2_b32 v2, v12, v13 offset0:64 offset1:96
	ds_write2_b32 v3, v28, v29 offset0:64 offset1:96
	v_add_u32_e32 v2, 0xc00, v74
	v_add_u32_e32 v3, 0x1c00, v74
	ds_write2_b32 v2, v14, v15 offset1:32
	ds_write2_b32 v3, v30, v31 offset1:32
	ds_write2_b32 v2, v16, v17 offset0:64 offset1:96
	ds_write2_b32 v3, v32, v33 offset0:64 offset1:96
	s_waitcnt lgkmcnt(0)
	s_barrier
	ds_read2st64_b32 v[2:3], v76 offset1:32
	ds_read2st64_b32 v[4:5], v76 offset0:64 offset1:96
	ds_read2st64_b32 v[6:7], v76 offset0:128 offset1:160
	s_waitcnt lgkmcnt(2)
	v_add_f32_e32 v2, 0, v2
	v_add_f32_e32 v8, v2, v3
	ds_read2st64_b32 v[2:3], v76 offset0:192 offset1:224
	s_waitcnt lgkmcnt(2)
	v_add_f32_e32 v4, v8, v4
	v_add_f32_e32 v4, v4, v5
	s_waitcnt lgkmcnt(1)
	v_add_f32_e32 v4, v4, v6
	v_add_f32_e32 v4, v4, v7
	s_waitcnt lgkmcnt(0)
	v_add_f32_e32 v2, v4, v2
	v_add_f32_e32 v14, v2, v3
	ds_read_b64 v[2:3], v138
	ds_read2_b32 v[4:5], v75 offset1:32
	ds_read2st64_b32 v[6:7], v78 offset1:32
	ds_read_b64 v[8:9], v139
	ds_read_b64 v[10:11], v140
	ds_read_b64 v[12:13], v141
	s_waitcnt lgkmcnt(4)
	v_fma_f32 v2, -v2, v4, v14
	v_fma_f32 v2, v3, v2, v5
	ds_write_b32 v77, v2
	ds_read2st64_b32 v[2:3], v78 offset0:64 offset1:96
	ds_read2st64_b32 v[14:15], v78 offset0:128 offset1:160
	s_waitcnt lgkmcnt(6)
	v_add_f32_e32 v6, 0, v6
	v_add_f32_e32 v16, v6, v7
	ds_read2st64_b32 v[6:7], v78 offset0:192 offset1:224
	s_waitcnt lgkmcnt(2)
	v_add_f32_e32 v2, v16, v2
	v_add_f32_e32 v2, v2, v3
	s_waitcnt lgkmcnt(1)
	v_add_f32_e32 v2, v2, v14
	v_add_f32_e32 v2, v2, v15
	s_waitcnt lgkmcnt(0)
	v_add_f32_e32 v2, v2, v6
	v_add_f32_e32 v6, v2, v7
	ds_read2st64_b32 v[2:3], v80 offset1:32
	v_fma_f32 v6, -v4, v8, v6
	v_fma_f32 v6, v9, v6, v5
	ds_write_b32 v79, v6
	ds_read2st64_b32 v[6:7], v80 offset0:64 offset1:96
	ds_read2st64_b32 v[8:9], v80 offset0:128 offset1:160
	s_waitcnt lgkmcnt(3)
	v_add_f32_e32 v2, 0, v2
	v_add_f32_e32 v14, v2, v3
	ds_read2st64_b32 v[2:3], v80 offset0:192 offset1:224
	s_waitcnt lgkmcnt(2)
	v_add_f32_e32 v6, v14, v6
	v_add_f32_e32 v6, v6, v7
	s_waitcnt lgkmcnt(1)
	v_add_f32_e32 v6, v6, v8
	v_add_f32_e32 v6, v6, v9
	s_waitcnt lgkmcnt(0)
	v_add_f32_e32 v2, v6, v2
	v_add_f32_e32 v6, v2, v3
	ds_read2st64_b32 v[2:3], v82 offset1:32
	v_fma_f32 v6, -v4, v10, v6
	v_fma_f32 v6, v11, v6, v5
	ds_write_b32 v81, v6
	ds_read2st64_b32 v[6:7], v82 offset0:64 offset1:96
	ds_read2st64_b32 v[8:9], v82 offset0:128 offset1:160
	s_waitcnt lgkmcnt(3)
	v_add_f32_e32 v2, 0, v2
	v_add_f32_e32 v10, v2, v3
	ds_read2st64_b32 v[2:3], v82 offset0:192 offset1:224
	s_waitcnt lgkmcnt(2)
	v_add_f32_e32 v6, v10, v6
	v_add_f32_e32 v6, v6, v7
	s_waitcnt lgkmcnt(1)
	v_add_f32_e32 v6, v6, v8
	v_add_f32_e32 v6, v6, v9
	s_waitcnt lgkmcnt(0)
	v_add_f32_e32 v2, v6, v2
	v_add_f32_e32 v2, v2, v3
	v_fma_f32 v2, -v4, v12, v2
	v_fmac_f32_e32 v5, v13, v2
	ds_write_b32 v83, v5
	s_waitcnt lgkmcnt(0)
	s_barrier
	s_and_saveexec_b64 s[36:37], s[82:83]
	s_cbranch_execz .LBB0_714
	ds_read_b32 v52, v84
	ds_read_b32 v34, v85
	ds_read_b32 v33, v86
	ds_read_b32 v32, v87
	ds_read_b32 v31, v88
	ds_read_b32 v30, v89
	ds_read_b32 v29, v90
	ds_read_b32 v28, v91
	ds_read_b32 v27, v92
	ds_read_b32 v26, v93
	ds_read_b32 v25, v94
	ds_read_b32 v24, v95
	ds_read_b32 v23, v96
	ds_read_b32 v22, v97
	ds_read_b32 v21, v98
	ds_read_b32 v20, v99
	ds_read_b32 v18, v100
	ds_read_b32 v17, v101
	ds_read_b32 v16, v102
	ds_read_b32 v15, v103
	ds_read_b32 v14, v104
	ds_read_b32 v13, v105
	ds_read_b32 v11, v106
	ds_read_b32 v10, v107
	ds_read_b32 v9, v108
	ds_read_b32 v8, v109
	ds_read_b32 v7, v110
	ds_read_b32 v6, v111
	ds_read_b32 v5, v112
	ds_read_b32 v4, v113
	ds_read_b32 v3, v114
	ds_read_b32 v2, v115
	s_waitcnt lgkmcnt(14)
	v_cmp_lg_f32_e32 vcc, s48, v52
	s_nop 1
	v_cndmask_b32_e32 v12, v143, v52, vcc
	v_cmp_gt_f32_e32 vcc, v34, v12
	s_nop 1
	v_cndmask_b32_e32 v12, v12, v34, vcc
	v_cndmask_b32_e64 v19, 0, 1, vcc
	v_cmp_gt_f32_e32 vcc, v33, v12
	s_nop 1
	v_cndmask_b32_e32 v12, v12, v33, vcc
	v_cndmask_b32_e64 v19, v19, 2, vcc
	v_cmp_gt_f32_e32 vcc, v32, v12
	s_nop 1
	v_cndmask_b32_e32 v12, v12, v32, vcc
	v_cndmask_b32_e64 v19, v19, 3, vcc
	v_cmp_gt_f32_e32 vcc, v31, v12
	s_nop 1
	v_cndmask_b32_e32 v12, v12, v31, vcc
	v_cndmask_b32_e64 v19, v19, 4, vcc
	v_cmp_gt_f32_e32 vcc, v30, v12
	s_nop 1
	v_cndmask_b32_e32 v12, v12, v30, vcc
	v_cndmask_b32_e64 v19, v19, 5, vcc
	v_cmp_gt_f32_e32 vcc, v29, v12
	s_nop 1
	v_cndmask_b32_e32 v12, v12, v29, vcc
	v_cndmask_b32_e64 v19, v19, 6, vcc
	v_cmp_gt_f32_e32 vcc, v28, v12
	s_nop 1
	v_cndmask_b32_e32 v12, v12, v28, vcc
	v_cndmask_b32_e64 v19, v19, 7, vcc
	v_cmp_gt_f32_e32 vcc, v27, v12
	s_nop 1
	v_cndmask_b32_e32 v12, v12, v27, vcc
	v_cndmask_b32_e64 v19, v19, 8, vcc
	v_cmp_gt_f32_e32 vcc, v26, v12
	s_nop 1
	v_cndmask_b32_e32 v12, v12, v26, vcc
	v_cndmask_b32_e64 v19, v19, 9, vcc
	v_cmp_gt_f32_e32 vcc, v25, v12
	s_nop 1
	v_cndmask_b32_e32 v12, v12, v25, vcc
	v_cndmask_b32_e64 v19, v19, 10, vcc
	v_cmp_gt_f32_e32 vcc, v24, v12
	s_nop 1
	v_cndmask_b32_e32 v12, v12, v24, vcc
	v_cndmask_b32_e64 v19, v19, 11, vcc
	v_cmp_gt_f32_e32 vcc, v23, v12
	s_nop 1
	v_cndmask_b32_e32 v12, v12, v23, vcc
	v_cndmask_b32_e64 v19, v19, 12, vcc
	v_cmp_gt_f32_e32 vcc, v22, v12
	s_nop 1
	v_cndmask_b32_e32 v12, v12, v22, vcc
	v_cndmask_b32_e64 v19, v19, 13, vcc
	v_cmp_gt_f32_e32 vcc, v21, v12
	s_nop 1
	v_cndmask_b32_e32 v12, v12, v21, vcc
	v_cndmask_b32_e64 v19, v19, 14, vcc
	v_cmp_gt_f32_e32 vcc, v20, v12
	s_nop 1
	v_cndmask_b32_e32 v12, v12, v20, vcc
	v_cndmask_b32_e64 v19, v19, 15, vcc
	v_cmp_gt_f32_e32 vcc, v18, v12
	s_nop 1
	v_cndmask_b32_e32 v12, v12, v18, vcc
	v_cndmask_b32_e64 v19, v19, 16, vcc
	v_cmp_gt_f32_e32 vcc, v17, v12
	s_nop 1
	v_cndmask_b32_e32 v12, v12, v17, vcc
	v_cndmask_b32_e64 v19, v19, 17, vcc
	s_waitcnt lgkmcnt(13)
	v_cmp_gt_f32_e32 vcc, v16, v12
	s_nop 1
	v_cndmask_b32_e32 v12, v12, v16, vcc
	v_cndmask_b32_e64 v19, v19, 18, vcc
	s_waitcnt lgkmcnt(12)
	v_cmp_gt_f32_e32 vcc, v15, v12
	s_nop 1
	v_cndmask_b32_e32 v12, v12, v15, vcc
	v_cndmask_b32_e64 v19, v19, 19, vcc
	s_waitcnt lgkmcnt(11)
	v_cmp_gt_f32_e32 vcc, v14, v12
	s_nop 1
	v_cndmask_b32_e32 v12, v12, v14, vcc
	v_cndmask_b32_e64 v19, v19, 20, vcc
	s_waitcnt lgkmcnt(10)
	v_cmp_gt_f32_e32 vcc, v13, v12
	s_nop 1
	v_cndmask_b32_e32 v12, v12, v13, vcc
	v_cndmask_b32_e64 v19, v19, 21, vcc
	s_waitcnt lgkmcnt(9)
	v_cmp_gt_f32_e32 vcc, v11, v12
	s_nop 1
	v_cndmask_b32_e32 v12, v12, v11, vcc
	v_cndmask_b32_e64 v19, v19, 22, vcc
	s_waitcnt lgkmcnt(8)
	v_cmp_gt_f32_e32 vcc, v10, v12
	s_nop 1
	v_cndmask_b32_e32 v12, v12, v10, vcc
	v_cndmask_b32_e64 v19, v19, 23, vcc
	s_waitcnt lgkmcnt(7)
	v_cmp_gt_f32_e32 vcc, v9, v12
	s_nop 1
	v_cndmask_b32_e32 v12, v12, v9, vcc
	v_cndmask_b32_e64 v19, v19, 24, vcc
	s_waitcnt lgkmcnt(6)
	v_cmp_gt_f32_e32 vcc, v8, v12
	s_nop 1
	v_cndmask_b32_e32 v12, v12, v8, vcc
	v_cndmask_b32_e64 v19, v19, 25, vcc
	s_waitcnt lgkmcnt(5)
	v_cmp_gt_f32_e32 vcc, v7, v12
	s_nop 1
	v_cndmask_b32_e32 v12, v12, v7, vcc
	v_cndmask_b32_e64 v19, v19, 26, vcc
	s_waitcnt lgkmcnt(4)
	v_cmp_gt_f32_e32 vcc, v6, v12
	s_nop 1
	v_cndmask_b32_e32 v12, v12, v6, vcc
	v_cndmask_b32_e64 v19, v19, 27, vcc
	s_waitcnt lgkmcnt(3)
	v_cmp_gt_f32_e32 vcc, v5, v12
	s_nop 1
	v_cndmask_b32_e32 v12, v12, v5, vcc
	v_cndmask_b32_e64 v19, v19, 28, vcc
	s_waitcnt lgkmcnt(2)
	v_cmp_gt_f32_e32 vcc, v4, v12
	s_nop 1
	v_cndmask_b32_e32 v12, v12, v4, vcc
	v_cndmask_b32_e64 v19, v19, 29, vcc
	s_waitcnt lgkmcnt(1)
	v_cmp_gt_f32_e32 vcc, v3, v12
	s_nop 1
	v_cndmask_b32_e32 v53, v12, v3, vcc
	v_cndmask_b32_e64 v19, v19, 30, vcc
	s_waitcnt lgkmcnt(0)
	v_cmp_gt_f32_e32 vcc, v2, v53
	s_nop 1
	v_cndmask_b32_e64 v12, v19, 31, vcc
	v_cndmask_b32_e32 v19, v53, v2, vcc
	v_cmp_eq_u32_e64 s[12:13], 0, v12
	v_cmp_nlg_f32_e32 vcc, s48, v52
	v_lshlrev_b32_e64 v53, v12, 1
	s_or_b64 s[12:13], s[12:13], vcc
	v_cndmask_b32_e64 v54, v52, v143, s[12:13]
	v_and_b32_e32 v55, 2, v53
	v_cmp_eq_u32_e64 s[12:13], 0, v55
	v_cmp_gt_f32_e64 s[14:15], v34, v54
	s_and_b64 s[12:13], s[12:13], s[14:15]
	v_cndmask_b32_e64 v54, v54, v34, s[12:13]
	v_and_b32_e32 v56, 4, v53
	v_cndmask_b32_e64 v55, 0, 1, s[12:13]
	v_cmp_eq_u32_e64 s[12:13], 0, v56
	v_cmp_gt_f32_e64 s[14:15], v33, v54
	s_and_b64 s[12:13], s[12:13], s[14:15]
	v_cndmask_b32_e64 v54, v54, v33, s[12:13]
	v_and_b32_e32 v56, 8, v53
	v_cndmask_b32_e64 v55, v55, 2, s[12:13]
	v_cmp_eq_u32_e64 s[12:13], 0, v56
	v_cmp_gt_f32_e64 s[14:15], v32, v54
	s_and_b64 s[12:13], s[12:13], s[14:15]
	v_cndmask_b32_e64 v54, v54, v32, s[12:13]
	v_and_b32_e32 v56, 16, v53
	v_cndmask_b32_e64 v55, v55, 3, s[12:13]
	v_cmp_eq_u32_e64 s[12:13], 0, v56
	v_cmp_gt_f32_e64 s[14:15], v31, v54
	s_and_b64 s[12:13], s[12:13], s[14:15]
	v_cndmask_b32_e64 v54, v54, v31, s[12:13]
	v_and_b32_e32 v56, 32, v53
	v_cndmask_b32_e64 v55, v55, 4, s[12:13]
	v_cmp_eq_u32_e64 s[12:13], 0, v56
	v_cmp_gt_f32_e64 s[14:15], v30, v54
	s_and_b64 s[12:13], s[12:13], s[14:15]
	v_cndmask_b32_e64 v54, v54, v30, s[12:13]
	v_and_b32_e32 v56, 64, v53
	v_cndmask_b32_e64 v55, v55, 5, s[12:13]
	v_cmp_eq_u32_e64 s[12:13], 0, v56
	v_cmp_gt_f32_e64 s[14:15], v29, v54
	s_and_b64 s[12:13], s[12:13], s[14:15]
	v_cndmask_b32_e64 v54, v54, v29, s[12:13]
	v_and_b32_e32 v56, 0x80, v53
	v_cndmask_b32_e64 v55, v55, 6, s[12:13]
	v_cmp_eq_u32_e64 s[12:13], 0, v56
	v_cmp_gt_f32_e64 s[14:15], v28, v54
	s_and_b64 s[12:13], s[12:13], s[14:15]
	v_cndmask_b32_e64 v54, v54, v28, s[12:13]
	v_and_b32_e32 v56, 0x100, v53
	v_cndmask_b32_e64 v55, v55, 7, s[12:13]
	v_cmp_eq_u32_e64 s[12:13], 0, v56
	v_cmp_gt_f32_e64 s[14:15], v27, v54
	s_and_b64 s[12:13], s[12:13], s[14:15]
	v_cndmask_b32_e64 v54, v54, v27, s[12:13]
	v_and_b32_e32 v56, 0x200, v53
	v_cndmask_b32_e64 v55, v55, 8, s[12:13]
	v_cmp_eq_u32_e64 s[12:13], 0, v56
	v_cmp_gt_f32_e64 s[14:15], v26, v54
	s_and_b64 s[12:13], s[12:13], s[14:15]
	v_cndmask_b32_e64 v54, v54, v26, s[12:13]
	v_and_b32_e32 v56, 0x400, v53
	v_cndmask_b32_e64 v55, v55, 9, s[12:13]
	v_cmp_eq_u32_e64 s[12:13], 0, v56
	v_cmp_gt_f32_e64 s[14:15], v25, v54
	s_and_b64 s[12:13], s[12:13], s[14:15]
	v_cndmask_b32_e64 v54, v54, v25, s[12:13]
	v_and_b32_e32 v56, 0x800, v53
	v_cndmask_b32_e64 v55, v55, 10, s[12:13]
	v_cmp_eq_u32_e64 s[12:13], 0, v56
	v_cmp_gt_f32_e64 s[14:15], v24, v54
	s_and_b64 s[12:13], s[12:13], s[14:15]
	v_cndmask_b32_e64 v54, v54, v24, s[12:13]
	v_and_b32_e32 v56, 0x1000, v53
	v_cndmask_b32_e64 v55, v55, 11, s[12:13]
	v_cmp_eq_u32_e64 s[12:13], 0, v56
	v_cmp_gt_f32_e64 s[14:15], v23, v54
	s_and_b64 s[12:13], s[12:13], s[14:15]
	v_cndmask_b32_e64 v54, v54, v23, s[12:13]
	v_and_b32_e32 v56, 0x2000, v53
	v_cndmask_b32_e64 v55, v55, 12, s[12:13]
	v_cmp_eq_u32_e64 s[12:13], 0, v56
	v_cmp_gt_f32_e64 s[14:15], v22, v54
	s_and_b64 s[12:13], s[12:13], s[14:15]
	v_cndmask_b32_e64 v54, v54, v22, s[12:13]
	v_and_b32_e32 v56, 0x4000, v53
	v_cndmask_b32_e64 v55, v55, 13, s[12:13]
	v_cmp_eq_u32_e64 s[12:13], 0, v56
	v_cmp_gt_f32_e64 s[14:15], v21, v54
	s_and_b64 s[12:13], s[12:13], s[14:15]
	v_cndmask_b32_e64 v54, v54, v21, s[12:13]
	v_and_b32_e32 v56, 0x8000, v53
	v_cndmask_b32_e64 v55, v55, 14, s[12:13]
	v_cmp_eq_u32_e64 s[12:13], 0, v56
	v_cmp_gt_f32_e64 s[14:15], v20, v54
	s_and_b64 s[12:13], s[12:13], s[14:15]
	v_cndmask_b32_e64 v54, v54, v20, s[12:13]
	v_and_b32_e32 v56, 0x10000, v53
	v_cndmask_b32_e64 v55, v55, 15, s[12:13]
	v_cmp_eq_u32_e64 s[12:13], 0, v56
	v_cmp_gt_f32_e64 s[14:15], v18, v54
	s_and_b64 s[12:13], s[12:13], s[14:15]
	v_cndmask_b32_e64 v54, v54, v18, s[12:13]
	v_and_b32_e32 v56, 0x20000, v53
	v_cndmask_b32_e64 v55, v55, 16, s[12:13]
	v_cmp_eq_u32_e64 s[12:13], 0, v56
	v_cmp_gt_f32_e64 s[14:15], v17, v54
	s_and_b64 s[12:13], s[12:13], s[14:15]
	v_cndmask_b32_e64 v54, v54, v17, s[12:13]
	v_and_b32_e32 v56, 0x40000, v53
	v_cndmask_b32_e64 v55, v55, 17, s[12:13]
	v_cmp_eq_u32_e64 s[12:13], 0, v56
	v_cmp_gt_f32_e64 s[14:15], v16, v54
	s_and_b64 s[12:13], s[12:13], s[14:15]
	v_cndmask_b32_e64 v54, v54, v16, s[12:13]
	v_and_b32_e32 v56, 0x80000, v53
	v_cndmask_b32_e64 v55, v55, 18, s[12:13]
	v_cmp_eq_u32_e64 s[12:13], 0, v56
	v_cmp_gt_f32_e64 s[14:15], v15, v54
	s_and_b64 s[12:13], s[12:13], s[14:15]
	v_cndmask_b32_e64 v54, v54, v15, s[12:13]
	v_and_b32_e32 v56, 0x100000, v53
	v_cndmask_b32_e64 v55, v55, 19, s[12:13]
	v_cmp_eq_u32_e64 s[12:13], 0, v56
	v_cmp_gt_f32_e64 s[14:15], v14, v54
	s_and_b64 s[12:13], s[12:13], s[14:15]
	v_cndmask_b32_e64 v54, v54, v14, s[12:13]
	v_and_b32_e32 v56, 0x200000, v53
	v_cndmask_b32_e64 v55, v55, 20, s[12:13]
	v_cmp_eq_u32_e64 s[12:13], 0, v56
	v_cmp_gt_f32_e64 s[14:15], v13, v54
	s_and_b64 s[12:13], s[12:13], s[14:15]
	v_cndmask_b32_e64 v54, v54, v13, s[12:13]
	v_and_b32_e32 v56, 0x400000, v53
	v_cndmask_b32_e64 v55, v55, 21, s[12:13]
	v_cmp_eq_u32_e64 s[12:13], 0, v56
	v_cmp_gt_f32_e64 s[14:15], v11, v54
	s_and_b64 s[12:13], s[12:13], s[14:15]
	v_cndmask_b32_e64 v54, v54, v11, s[12:13]
	v_and_b32_e32 v56, 0x800000, v53
	v_cndmask_b32_e64 v55, v55, 22, s[12:13]
	v_cmp_eq_u32_e64 s[12:13], 0, v56
	v_cmp_gt_f32_e64 s[14:15], v10, v54
	s_and_b64 s[12:13], s[12:13], s[14:15]
	v_cndmask_b32_e64 v54, v54, v10, s[12:13]
	v_and_b32_e32 v56, 0x1000000, v53
	v_cndmask_b32_e64 v55, v55, 23, s[12:13]
	v_cmp_eq_u32_e64 s[12:13], 0, v56
	v_cmp_gt_f32_e64 s[14:15], v9, v54
	s_and_b64 s[12:13], s[12:13], s[14:15]
	v_cndmask_b32_e64 v54, v54, v9, s[12:13]
	v_and_b32_e32 v56, 0x2000000, v53
	v_cndmask_b32_e64 v55, v55, 24, s[12:13]
	v_cmp_eq_u32_e64 s[12:13], 0, v56
	v_cmp_gt_f32_e64 s[14:15], v8, v54
	s_and_b64 s[12:13], s[12:13], s[14:15]
	v_cndmask_b32_e64 v54, v54, v8, s[12:13]
	v_and_b32_e32 v56, 0x4000000, v53
	v_cndmask_b32_e64 v55, v55, 25, s[12:13]
	v_cmp_eq_u32_e64 s[12:13], 0, v56
	v_cmp_gt_f32_e64 s[14:15], v7, v54
	s_and_b64 s[12:13], s[12:13], s[14:15]
	v_cndmask_b32_e64 v54, v54, v7, s[12:13]
	v_and_b32_e32 v56, 0x8000000, v53
	v_cndmask_b32_e64 v55, v55, 26, s[12:13]
	v_cmp_eq_u32_e64 s[12:13], 0, v56
	v_cmp_gt_f32_e64 s[14:15], v6, v54
	s_and_b64 s[12:13], s[12:13], s[14:15]
	v_cndmask_b32_e64 v54, v54, v6, s[12:13]
	v_and_b32_e32 v56, 0x10000000, v53
	v_cndmask_b32_e64 v55, v55, 27, s[12:13]
	v_cmp_eq_u32_e64 s[12:13], 0, v56
	v_cmp_gt_f32_e64 s[14:15], v5, v54
	s_and_b64 s[12:13], s[12:13], s[14:15]
	v_cndmask_b32_e64 v54, v54, v5, s[12:13]
	v_and_b32_e32 v56, 0x20000000, v53
	v_cndmask_b32_e64 v55, v55, 28, s[12:13]
	v_cmp_eq_u32_e64 s[12:13], 0, v56
	v_cmp_gt_f32_e64 s[14:15], v4, v54
	s_and_b64 s[12:13], s[12:13], s[14:15]
	v_cndmask_b32_e64 v54, v54, v4, s[12:13]
	v_and_b32_e32 v56, 2.0, v53
	v_cndmask_b32_e64 v55, v55, 29, s[12:13]
	v_cmp_eq_u32_e64 s[12:13], 0, v56
	v_cmp_gt_f32_e64 s[14:15], v3, v54
	s_and_b64 s[12:13], s[12:13], s[14:15]
	v_cndmask_b32_e64 v54, v54, v3, s[12:13]
	v_cndmask_b32_e64 v55, v55, 30, s[12:13]
	v_cmp_ne_u32_e64 s[12:13], 31, v12
	v_cmp_gt_f32_e64 s[14:15], v2, v54
	s_and_b64 s[12:13], s[12:13], s[14:15]
	v_cndmask_b32_e64 v55, v55, 31, s[12:13]
	v_lshl_or_b32 v53, 1, v55, v53
	v_and_b32_e32 v56, 1, v53
	v_cndmask_b32_e64 v54, v54, v2, s[12:13]
	v_cmp_eq_u32_e64 s[12:13], 1, v56
	s_or_b64 s[12:13], s[12:13], vcc
	v_and_b32_e32 v57, 2, v53
	v_cndmask_b32_e64 v56, v52, v143, s[12:13]
	v_cmp_eq_u32_e64 s[12:13], 0, v57
	v_cmp_gt_f32_e64 s[14:15], v34, v56
	s_and_b64 s[12:13], s[12:13], s[14:15]
	v_cndmask_b32_e64 v56, v56, v34, s[12:13]
	v_and_b32_e32 v58, 4, v53
	v_cndmask_b32_e64 v57, 0, 1, s[12:13]
	v_cmp_eq_u32_e64 s[12:13], 0, v58
	v_cmp_gt_f32_e64 s[14:15], v33, v56
	s_and_b64 s[12:13], s[12:13], s[14:15]
	v_cndmask_b32_e64 v56, v56, v33, s[12:13]
	v_and_b32_e32 v58, 8, v53
	v_cndmask_b32_e64 v57, v57, 2, s[12:13]
	v_cmp_eq_u32_e64 s[12:13], 0, v58
	v_cmp_gt_f32_e64 s[14:15], v32, v56
	s_and_b64 s[12:13], s[12:13], s[14:15]
	v_cndmask_b32_e64 v56, v56, v32, s[12:13]
	v_and_b32_e32 v58, 16, v53
	v_cndmask_b32_e64 v57, v57, 3, s[12:13]
	v_cmp_eq_u32_e64 s[12:13], 0, v58
	v_cmp_gt_f32_e64 s[14:15], v31, v56
	s_and_b64 s[12:13], s[12:13], s[14:15]
	v_cndmask_b32_e64 v56, v56, v31, s[12:13]
	v_and_b32_e32 v58, 32, v53
	v_cndmask_b32_e64 v57, v57, 4, s[12:13]
	v_cmp_eq_u32_e64 s[12:13], 0, v58
	v_cmp_gt_f32_e64 s[14:15], v30, v56
	s_and_b64 s[12:13], s[12:13], s[14:15]
	v_cndmask_b32_e64 v56, v56, v30, s[12:13]
	v_and_b32_e32 v58, 64, v53
	v_cndmask_b32_e64 v57, v57, 5, s[12:13]
	v_cmp_eq_u32_e64 s[12:13], 0, v58
	v_cmp_gt_f32_e64 s[14:15], v29, v56
	s_and_b64 s[12:13], s[12:13], s[14:15]
	v_cndmask_b32_e64 v56, v56, v29, s[12:13]
	v_and_b32_e32 v58, 0x80, v53
	v_cndmask_b32_e64 v57, v57, 6, s[12:13]
	v_cmp_eq_u32_e64 s[12:13], 0, v58
	v_cmp_gt_f32_e64 s[14:15], v28, v56
	s_and_b64 s[12:13], s[12:13], s[14:15]
	v_cndmask_b32_e64 v56, v56, v28, s[12:13]
	v_and_b32_e32 v58, 0x100, v53
	v_cndmask_b32_e64 v57, v57, 7, s[12:13]
	v_cmp_eq_u32_e64 s[12:13], 0, v58
	v_cmp_gt_f32_e64 s[14:15], v27, v56
	s_and_b64 s[12:13], s[12:13], s[14:15]
	v_cndmask_b32_e64 v56, v56, v27, s[12:13]
	v_and_b32_e32 v58, 0x200, v53
	v_cndmask_b32_e64 v57, v57, 8, s[12:13]
	v_cmp_eq_u32_e64 s[12:13], 0, v58
	v_cmp_gt_f32_e64 s[14:15], v26, v56
	s_and_b64 s[12:13], s[12:13], s[14:15]
	v_cndmask_b32_e64 v56, v56, v26, s[12:13]
	v_and_b32_e32 v58, 0x400, v53
	v_cndmask_b32_e64 v57, v57, 9, s[12:13]
	v_cmp_eq_u32_e64 s[12:13], 0, v58
	v_cmp_gt_f32_e64 s[14:15], v25, v56
	s_and_b64 s[12:13], s[12:13], s[14:15]
	v_cndmask_b32_e64 v56, v56, v25, s[12:13]
	v_and_b32_e32 v58, 0x800, v53
	v_cndmask_b32_e64 v57, v57, 10, s[12:13]
	v_cmp_eq_u32_e64 s[12:13], 0, v58
	v_cmp_gt_f32_e64 s[14:15], v24, v56
	s_and_b64 s[12:13], s[12:13], s[14:15]
	v_cndmask_b32_e64 v56, v56, v24, s[12:13]
	v_and_b32_e32 v58, 0x1000, v53
	v_cndmask_b32_e64 v57, v57, 11, s[12:13]
	v_cmp_eq_u32_e64 s[12:13], 0, v58
	v_cmp_gt_f32_e64 s[14:15], v23, v56
	s_and_b64 s[12:13], s[12:13], s[14:15]
	v_cndmask_b32_e64 v56, v56, v23, s[12:13]
	v_and_b32_e32 v58, 0x2000, v53
	v_cndmask_b32_e64 v57, v57, 12, s[12:13]
	v_cmp_eq_u32_e64 s[12:13], 0, v58
	v_cmp_gt_f32_e64 s[14:15], v22, v56
	s_and_b64 s[12:13], s[12:13], s[14:15]
	v_cndmask_b32_e64 v56, v56, v22, s[12:13]
	v_and_b32_e32 v58, 0x4000, v53
	v_cndmask_b32_e64 v57, v57, 13, s[12:13]
	v_cmp_eq_u32_e64 s[12:13], 0, v58
	v_cmp_gt_f32_e64 s[14:15], v21, v56
	s_and_b64 s[12:13], s[12:13], s[14:15]
	v_cndmask_b32_e64 v56, v56, v21, s[12:13]
	v_and_b32_e32 v58, 0x8000, v53
	v_cndmask_b32_e64 v57, v57, 14, s[12:13]
	v_cmp_eq_u32_e64 s[12:13], 0, v58
	v_cmp_gt_f32_e64 s[14:15], v20, v56
	s_and_b64 s[12:13], s[12:13], s[14:15]
	v_cndmask_b32_e64 v56, v56, v20, s[12:13]
	v_and_b32_e32 v58, 0x10000, v53
	v_cndmask_b32_e64 v57, v57, 15, s[12:13]
	v_cmp_eq_u32_e64 s[12:13], 0, v58
	v_cmp_gt_f32_e64 s[14:15], v18, v56
	s_and_b64 s[12:13], s[12:13], s[14:15]
	v_cndmask_b32_e64 v56, v56, v18, s[12:13]
	v_and_b32_e32 v58, 0x20000, v53
	v_cndmask_b32_e64 v57, v57, 16, s[12:13]
	v_cmp_eq_u32_e64 s[12:13], 0, v58
	v_cmp_gt_f32_e64 s[14:15], v17, v56
	s_and_b64 s[12:13], s[12:13], s[14:15]
	v_cndmask_b32_e64 v56, v56, v17, s[12:13]
	v_and_b32_e32 v58, 0x40000, v53
	v_cndmask_b32_e64 v57, v57, 17, s[12:13]
	v_cmp_eq_u32_e64 s[12:13], 0, v58
	v_cmp_gt_f32_e64 s[14:15], v16, v56
	s_and_b64 s[12:13], s[12:13], s[14:15]
	v_cndmask_b32_e64 v56, v56, v16, s[12:13]
	v_and_b32_e32 v58, 0x80000, v53
	v_cndmask_b32_e64 v57, v57, 18, s[12:13]
	v_cmp_eq_u32_e64 s[12:13], 0, v58
	v_cmp_gt_f32_e64 s[14:15], v15, v56
	s_and_b64 s[12:13], s[12:13], s[14:15]
	v_cndmask_b32_e64 v56, v56, v15, s[12:13]
	v_and_b32_e32 v58, 0x100000, v53
	v_cndmask_b32_e64 v57, v57, 19, s[12:13]
	v_cmp_eq_u32_e64 s[12:13], 0, v58
	v_cmp_gt_f32_e64 s[14:15], v14, v56
	s_and_b64 s[12:13], s[12:13], s[14:15]
	v_cndmask_b32_e64 v56, v56, v14, s[12:13]
	v_and_b32_e32 v58, 0x200000, v53
	v_cndmask_b32_e64 v57, v57, 20, s[12:13]
	v_cmp_eq_u32_e64 s[12:13], 0, v58
	v_cmp_gt_f32_e64 s[14:15], v13, v56
	s_and_b64 s[12:13], s[12:13], s[14:15]
	v_cndmask_b32_e64 v56, v56, v13, s[12:13]
	v_and_b32_e32 v58, 0x400000, v53
	v_cndmask_b32_e64 v57, v57, 21, s[12:13]
	v_cmp_eq_u32_e64 s[12:13], 0, v58
	v_cmp_gt_f32_e64 s[14:15], v11, v56
	s_and_b64 s[12:13], s[12:13], s[14:15]
	v_cndmask_b32_e64 v56, v56, v11, s[12:13]
	v_and_b32_e32 v58, 0x800000, v53
	v_cndmask_b32_e64 v57, v57, 22, s[12:13]
	v_cmp_eq_u32_e64 s[12:13], 0, v58
	v_cmp_gt_f32_e64 s[14:15], v10, v56
	s_and_b64 s[12:13], s[12:13], s[14:15]
	v_cndmask_b32_e64 v56, v56, v10, s[12:13]
	v_and_b32_e32 v58, 0x1000000, v53
	v_cndmask_b32_e64 v57, v57, 23, s[12:13]
	v_cmp_eq_u32_e64 s[12:13], 0, v58
	v_cmp_gt_f32_e64 s[14:15], v9, v56
	s_and_b64 s[12:13], s[12:13], s[14:15]
	v_cndmask_b32_e64 v56, v56, v9, s[12:13]
	v_and_b32_e32 v58, 0x2000000, v53
	v_cndmask_b32_e64 v57, v57, 24, s[12:13]
	v_cmp_eq_u32_e64 s[12:13], 0, v58
	v_cmp_gt_f32_e64 s[14:15], v8, v56
	s_and_b64 s[12:13], s[12:13], s[14:15]
	v_cndmask_b32_e64 v56, v56, v8, s[12:13]
	v_and_b32_e32 v58, 0x4000000, v53
	v_cndmask_b32_e64 v57, v57, 25, s[12:13]
	v_cmp_eq_u32_e64 s[12:13], 0, v58
	v_cmp_gt_f32_e64 s[14:15], v7, v56
	s_and_b64 s[12:13], s[12:13], s[14:15]
	v_cndmask_b32_e64 v56, v56, v7, s[12:13]
	v_and_b32_e32 v58, 0x8000000, v53
	v_cndmask_b32_e64 v57, v57, 26, s[12:13]
	v_cmp_eq_u32_e64 s[12:13], 0, v58
	v_cmp_gt_f32_e64 s[14:15], v6, v56
	s_and_b64 s[12:13], s[12:13], s[14:15]
	v_cndmask_b32_e64 v56, v56, v6, s[12:13]
	v_and_b32_e32 v58, 0x10000000, v53
	v_cndmask_b32_e64 v57, v57, 27, s[12:13]
	v_cmp_eq_u32_e64 s[12:13], 0, v58
	v_cmp_gt_f32_e64 s[14:15], v5, v56
	s_and_b64 s[12:13], s[12:13], s[14:15]
	v_cndmask_b32_e64 v56, v56, v5, s[12:13]
	v_and_b32_e32 v58, 0x20000000, v53
	v_cndmask_b32_e64 v57, v57, 28, s[12:13]
	v_cmp_eq_u32_e64 s[12:13], 0, v58
	v_cmp_gt_f32_e64 s[14:15], v4, v56
	s_and_b64 s[12:13], s[12:13], s[14:15]
	v_cndmask_b32_e64 v56, v56, v4, s[12:13]
	v_and_b32_e32 v58, 2.0, v53
	v_cndmask_b32_e64 v57, v57, 29, s[12:13]
	v_cmp_eq_u32_e64 s[12:13], 0, v58
	v_cmp_gt_f32_e64 s[14:15], v3, v56
	s_and_b64 s[12:13], s[12:13], s[14:15]
	v_cndmask_b32_e64 v56, v56, v3, s[12:13]
	v_cndmask_b32_e64 v57, v57, 30, s[12:13]
	v_cmp_lt_i32_e64 s[12:13], -1, v53
	v_cmp_gt_f32_e64 s[14:15], v2, v56
	s_and_b64 s[12:13], s[12:13], s[14:15]
	v_cndmask_b32_e64 v57, v57, 31, s[12:13]
	v_lshlrev_b32_e64 v58, v57, 1
	v_or_b32_e32 v59, v58, v53
	v_and_b32_e32 v60, 1, v59
	v_cndmask_b32_e64 v56, v56, v2, s[12:13]
	v_cmp_eq_u32_e64 s[12:13], 1, v60
	s_or_b64 vcc, s[12:13], vcc
	v_cndmask_b32_e32 v52, v52, v143, vcc
	v_bitop3_b32 v60, v58, 2, v53 bitop3:0xc8
	v_cmp_eq_u32_e32 vcc, 0, v60
	v_cmp_gt_f32_e64 s[12:13], v34, v52
	s_and_b64 vcc, vcc, s[12:13]
	v_cndmask_b32_e32 v34, v52, v34, vcc
	v_bitop3_b32 v52, v58, 4, v53 bitop3:0xc8
	v_cndmask_b32_e64 v60, 0, 1, vcc
	v_cmp_eq_u32_e32 vcc, 0, v52
	v_cmp_gt_f32_e64 s[12:13], v33, v34
	s_and_b64 vcc, vcc, s[12:13]
	v_cndmask_b32_e32 v33, v34, v33, vcc
	v_bitop3_b32 v34, v58, 8, v53 bitop3:0xc8
	v_cndmask_b32_e64 v52, v60, 2, vcc
	v_cmp_eq_u32_e32 vcc, 0, v34
	v_cmp_gt_f32_e64 s[12:13], v32, v33
	s_and_b64 vcc, vcc, s[12:13]
	v_cndmask_b32_e32 v32, v33, v32, vcc
	v_bitop3_b32 v33, v58, 16, v53 bitop3:0xc8
	v_cndmask_b32_e64 v34, v52, 3, vcc
	v_cmp_eq_u32_e32 vcc, 0, v33
	v_cmp_gt_f32_e64 s[12:13], v31, v32
	s_and_b64 vcc, vcc, s[12:13]
	v_cndmask_b32_e32 v31, v32, v31, vcc
	v_bitop3_b32 v32, v58, 32, v53 bitop3:0xc8
	v_cndmask_b32_e64 v33, v34, 4, vcc
	v_cmp_eq_u32_e32 vcc, 0, v32
	v_cmp_gt_f32_e64 s[12:13], v30, v31
	s_and_b64 vcc, vcc, s[12:13]
	v_cndmask_b32_e32 v30, v31, v30, vcc
	v_bitop3_b32 v31, v58, 64, v53 bitop3:0xc8
	v_cndmask_b32_e64 v32, v33, 5, vcc
	v_cmp_eq_u32_e32 vcc, 0, v31
	v_cmp_gt_f32_e64 s[12:13], v29, v30
	s_and_b64 vcc, vcc, s[12:13]
	v_cndmask_b32_e32 v29, v30, v29, vcc
	v_bitop3_b32 v30, v58, s49, v53 bitop3:0xc8
	v_cndmask_b32_e64 v31, v32, 6, vcc
	v_cmp_eq_u32_e32 vcc, 0, v30
	v_cmp_gt_f32_e64 s[12:13], v28, v29
	s_and_b64 vcc, vcc, s[12:13]
	v_cndmask_b32_e32 v28, v29, v28, vcc
	v_bitop3_b32 v29, v58, s39, v53 bitop3:0xc8
	v_cndmask_b32_e64 v30, v31, 7, vcc
	v_cmp_eq_u32_e32 vcc, 0, v29
	v_cmp_gt_f32_e64 s[12:13], v27, v28
	s_and_b64 vcc, vcc, s[12:13]
	s_movk_i32 s12, 0x200
	v_cndmask_b32_e32 v27, v28, v27, vcc
	v_bitop3_b32 v28, v58, s12, v53 bitop3:0xc8
	v_cndmask_b32_e64 v29, v30, 8, vcc
	v_cmp_eq_u32_e32 vcc, 0, v28
	v_cmp_gt_f32_e64 s[12:13], v26, v27
	s_and_b64 vcc, vcc, s[12:13]
	s_movk_i32 s12, 0x400
	v_cndmask_b32_e32 v26, v27, v26, vcc
	v_bitop3_b32 v27, v58, s12, v53 bitop3:0xc8
	v_cndmask_b32_e64 v28, v29, 9, vcc
	v_cmp_eq_u32_e32 vcc, 0, v27
	v_cmp_gt_f32_e64 s[12:13], v25, v26
	s_and_b64 vcc, vcc, s[12:13]
	v_cndmask_b32_e32 v25, v26, v25, vcc
	v_bitop3_b32 v26, v58, s3, v53 bitop3:0xc8
	v_cndmask_b32_e64 v27, v28, 10, vcc
	v_cmp_eq_u32_e32 vcc, 0, v26
	v_cmp_gt_f32_e64 s[12:13], v24, v25
	s_and_b64 vcc, vcc, s[12:13]
	v_cndmask_b32_e32 v24, v25, v24, vcc
	v_bitop3_b32 v25, v58, s50, v53 bitop3:0xc8
	v_cndmask_b32_e64 v26, v27, 11, vcc
	v_cmp_eq_u32_e32 vcc, 0, v25
	v_cmp_gt_f32_e64 s[12:13], v23, v24
	s_and_b64 vcc, vcc, s[12:13]
	v_cndmask_b32_e32 v23, v24, v23, vcc
	v_bitop3_b32 v24, v58, s51, v53 bitop3:0xc8
	v_cndmask_b32_e64 v25, v26, 12, vcc
	v_cmp_eq_u32_e32 vcc, 0, v24
	v_cmp_gt_f32_e64 s[12:13], v22, v23
	s_and_b64 vcc, vcc, s[12:13]
	v_cndmask_b32_e32 v22, v23, v22, vcc
	v_bitop3_b32 v23, v58, s52, v53 bitop3:0xc8
	v_cndmask_b32_e64 v24, v25, 13, vcc
	v_cmp_eq_u32_e32 vcc, 0, v23
	v_cmp_gt_f32_e64 s[12:13], v21, v22
	s_and_b64 vcc, vcc, s[12:13]
	v_cndmask_b32_e32 v21, v22, v21, vcc
	v_bitop3_b32 v22, v58, s53, v53 bitop3:0xc8
	v_cndmask_b32_e64 v23, v24, 14, vcc
	v_cmp_eq_u32_e32 vcc, 0, v22
	v_cmp_gt_f32_e64 s[12:13], v20, v21
	s_and_b64 vcc, vcc, s[12:13]
	s_mov_b32 s12, 0x10000
	v_cndmask_b32_e32 v20, v21, v20, vcc
	v_bitop3_b32 v21, v58, s12, v53 bitop3:0xc8
	v_cndmask_b32_e64 v22, v23, 15, vcc
	v_cmp_eq_u32_e32 vcc, 0, v21
	v_cmp_gt_f32_e64 s[12:13], v18, v20
	s_and_b64 vcc, vcc, s[12:13]
	v_cndmask_b32_e32 v18, v20, v18, vcc
	v_bitop3_b32 v20, v58, s54, v53 bitop3:0xc8
	v_cndmask_b32_e64 v21, v22, 16, vcc
	v_cmp_eq_u32_e32 vcc, 0, v20
	v_cmp_gt_f32_e64 s[12:13], v17, v18
	s_and_b64 vcc, vcc, s[12:13]
	v_cndmask_b32_e32 v17, v18, v17, vcc
	v_bitop3_b32 v18, v58, s55, v53 bitop3:0xc8
	v_cndmask_b32_e64 v20, v21, 17, vcc
	v_cmp_eq_u32_e32 vcc, 0, v18
	v_cmp_gt_f32_e64 s[12:13], v16, v17
	s_and_b64 vcc, vcc, s[12:13]
	v_cndmask_b32_e32 v16, v17, v16, vcc
	v_bitop3_b32 v17, v58, s56, v53 bitop3:0xc8
	v_cndmask_b32_e64 v18, v20, 18, vcc
	v_cmp_eq_u32_e32 vcc, 0, v17
	v_cmp_gt_f32_e64 s[12:13], v15, v16
	s_and_b64 vcc, vcc, s[12:13]
	v_cndmask_b32_e32 v15, v16, v15, vcc
	v_bitop3_b32 v16, v58, s57, v53 bitop3:0xc8
	v_cndmask_b32_e64 v17, v18, 19, vcc
	v_cmp_eq_u32_e32 vcc, 0, v16
	v_cmp_gt_f32_e64 s[12:13], v14, v15
	s_and_b64 vcc, vcc, s[12:13]
	v_cndmask_b32_e32 v14, v15, v14, vcc
	v_bitop3_b32 v15, v58, s58, v53 bitop3:0xc8
	v_cndmask_b32_e64 v16, v17, 20, vcc
	v_cmp_eq_u32_e32 vcc, 0, v15
	v_cmp_gt_f32_e64 s[12:13], v13, v14
	s_and_b64 vcc, vcc, s[12:13]
	v_cndmask_b32_e32 v13, v14, v13, vcc
	v_bitop3_b32 v14, v58, s59, v53 bitop3:0xc8
	v_cndmask_b32_e64 v15, v16, 21, vcc
	v_cmp_eq_u32_e32 vcc, 0, v14
	v_cmp_gt_f32_e64 s[12:13], v11, v13
	s_and_b64 vcc, vcc, s[12:13]
	v_cndmask_b32_e32 v11, v13, v11, vcc
	v_bitop3_b32 v13, v58, s60, v53 bitop3:0xc8
	v_cndmask_b32_e64 v14, v15, 22, vcc
	v_cmp_eq_u32_e32 vcc, 0, v13
	v_cmp_gt_f32_e64 s[12:13], v10, v11
	s_and_b64 vcc, vcc, s[12:13]
	v_cndmask_b32_e32 v10, v11, v10, vcc
	v_bitop3_b32 v11, v58, s61, v53 bitop3:0xc8
	v_cndmask_b32_e64 v13, v14, 23, vcc
	v_cmp_eq_u32_e32 vcc, 0, v11
	v_cmp_gt_f32_e64 s[12:13], v9, v10
	s_and_b64 vcc, vcc, s[12:13]
	v_cndmask_b32_e32 v9, v10, v9, vcc
	v_bitop3_b32 v10, v58, s62, v53 bitop3:0xc8
	v_cndmask_b32_e64 v11, v13, 24, vcc
	v_cmp_eq_u32_e32 vcc, 0, v10
	v_cmp_gt_f32_e64 s[12:13], v8, v9
	s_and_b64 vcc, vcc, s[12:13]
	v_cndmask_b32_e32 v8, v9, v8, vcc
	v_bitop3_b32 v9, v58, s63, v53 bitop3:0xc8
	v_cndmask_b32_e64 v10, v11, 25, vcc
	v_cmp_eq_u32_e32 vcc, 0, v9
	v_cmp_gt_f32_e64 s[12:13], v7, v8
	s_and_b64 vcc, vcc, s[12:13]
	v_cndmask_b32_e32 v7, v8, v7, vcc
	v_bitop3_b32 v8, v58, s64, v53 bitop3:0xc8
	v_cndmask_b32_e64 v9, v10, 26, vcc
	v_cmp_eq_u32_e32 vcc, 0, v8
	v_cmp_gt_f32_e64 s[12:13], v6, v7
	s_and_b64 vcc, vcc, s[12:13]
	v_cndmask_b32_e32 v6, v7, v6, vcc
	v_bitop3_b32 v7, v58, s65, v53 bitop3:0xc8
	v_cndmask_b32_e64 v8, v9, 27, vcc
	v_cmp_eq_u32_e32 vcc, 0, v7
	v_cmp_gt_f32_e64 s[12:13], v5, v6
	s_and_b64 vcc, vcc, s[12:13]
	v_cndmask_b32_e32 v5, v6, v5, vcc
	v_bitop3_b32 v6, v58, s66, v53 bitop3:0xc8
	v_cndmask_b32_e64 v7, v8, 28, vcc
	v_cmp_eq_u32_e32 vcc, 0, v6
	v_cmp_gt_f32_e64 s[12:13], v4, v5
	s_and_b64 vcc, vcc, s[12:13]
	v_cndmask_b32_e32 v4, v5, v4, vcc
	v_bitop3_b32 v5, v58, 2.0, v53 bitop3:0xc8
	v_cndmask_b32_e64 v6, v7, 29, vcc
	v_cmp_eq_u32_e32 vcc, 0, v5
	v_cmp_gt_f32_e64 s[12:13], v3, v4
	s_and_b64 vcc, vcc, s[12:13]
	v_cndmask_b32_e32 v3, v4, v3, vcc
	v_cndmask_b32_e64 v5, v6, 30, vcc
	v_cmp_lt_i32_e32 vcc, -1, v59
	v_cmp_gt_f32_e64 s[12:13], v2, v3
	s_and_b64 vcc, vcc, s[12:13]
	v_cndmask_b32_e32 v2, v3, v2, vcc
	v_sub_f32_e32 v3, v54, v19
	v_cndmask_b32_e64 v4, v5, 31, vcc
	v_mul_f32_e32 v3, 0x3fb8aa3b, v3
	v_sub_f32_e32 v5, v56, v19
	v_exp_f32_e32 v3, v3
	v_mul_f32_e32 v5, 0x3fb8aa3b, v5
	v_sub_f32_e32 v2, v2, v19
	v_exp_f32_e32 v5, v5
	v_mul_f32_e32 v2, 0x3fb8aa3b, v2
	v_exp_f32_e32 v2, v2
	v_add_f32_e32 v6, 1.0, v3
	v_add_f32_e32 v6, v6, v5
	v_add_f32_e32 v6, v6, v2
	v_div_scale_f32 v7, s[12:13], v6, v6, 1.0
	v_rcp_f32_e32 v8, v7
	s_nop 0
	v_fma_f32 v9, -v7, v8, 1.0
	v_fmac_f32_e32 v8, v9, v8
	v_div_scale_f32 v9, vcc, 1.0, v6, 1.0
	v_mul_f32_e32 v10, v9, v8
	v_fma_f32 v11, -v7, v10, v9
	v_fmac_f32_e32 v10, v11, v8
	v_fma_f32 v7, -v7, v10, v9
	v_div_fmas_f32 v7, v7, v8, v10
	v_div_fixup_f32 v6, v7, v6, 1.0
	ds_write_b32 v116, v12
	ds_write_b32 v117, v6
	v_lshl_add_u32 v7, v12, 2, s38
	ds_add_rtn_u32 v7, v7, v142
	v_mul_f32_e32 v3, v3, v6
	s_waitcnt lgkmcnt(0)
	ds_write_b32 v118, v7
	ds_write_b32 v119, v55
	ds_write_b32 v120, v3
	v_lshl_add_u32 v3, v55, 2, s38
	ds_add_rtn_u32 v3, v3, v142
	v_mul_f32_e32 v5, v5, v6
	s_waitcnt lgkmcnt(0)
	ds_write_b32 v121, v3
	ds_write_b32 v122, v57
	ds_write_b32 v123, v5
	v_lshl_add_u32 v3, v57, 2, s38
	ds_add_rtn_u32 v3, v3, v142
	v_mul_f32_e32 v2, v2, v6
	s_waitcnt lgkmcnt(0)
	ds_write_b32 v124, v3
	ds_write_b32 v125, v4
	ds_write_b32 v126, v2
	v_lshl_add_u32 v2, v4, 2, s38
	ds_add_rtn_u32 v2, v2, v142
	s_waitcnt lgkmcnt(0)
	ds_write_b32 v127, v2
